# expert-down piece loop: the redundant LDS drain in front of the first MFMA of every second piece replaced by s_nop 0 (same code placement)
# baseline (speedup 1.0000x reference)
.LBB0_789:
	s_add_i32 s19, s6, 1
	s_lshl_b32 s4, s19, 14
	s_and_b32 s4, s4, 0x1c000
	v_add_u32_e32 v100, s4, v206
	ds_read_b128 v[120:123], v100
	ds_read_b128 v[124:127], v100 offset:1024
	ds_read_b128 v[112:115], v100 offset:2048
	ds_read_b128 v[116:119], v100 offset:3072
	ds_read_b128 v[104:107], v100 offset:8192
	ds_read_b128 v[108:111], v100 offset:9216
	ds_read_b128 v[96:99], v100 offset:10240
	ds_read_b128 v[100:103], v100 offset:11264
	v_med3_f32 v210, v132, s7, v209
	v_med3_f32 v160, v133, s7, v209
	v_cvt_pk_fp8_f32 v210, v210, v160
	v_med3_f32 v160, v134, s7, v209
	v_med3_f32 v161, v135, s7, v209
	v_cvt_pk_fp8_f32 v210, v160, v161 op_sel:[0,0,1]
	s_nop 0
	v_mfma_f32_16x16x128_f8f6f4 v[160:163], v[0:7], v[64:71], 0
	v_mfma_f32_16x16x128_f8f6f4 v[164:167], v[8:15], v[64:71], 0
	v_med3_f32 v211, v128, s7, v209
	v_med3_f32 v168, v129, s7, v209
	v_cvt_pk_fp8_f32 v211, v211, v168
	v_med3_f32 v168, v130, s7, v209
	v_med3_f32 v169, v131, s7, v209
	v_cvt_pk_fp8_f32 v211, v168, v169 op_sel:[0,0,1]
	v_mfma_f32_16x16x128_f8f6f4 v[168:171], v[16:23], v[64:71], 0
	v_mfma_f32_16x16x128_f8f6f4 v[172:175], v[24:31], v[64:71], 0
	s_lshl_b32 s22, s6, 6
	s_add_i32 s4, s22, 0x3c0
	s_and_b32 s4, s4, 0x3c0
	v_lshl_add_u32 v176, s4, 2, v208
	ds_read2_b32 v[176:177], v176 offset1:16
	v_mov_b32_e32 v219, v197
	s_waitcnt lgkmcnt(0)
	v_mov_b32_e32 v196, v176
	v_mov_b32_e32 v218, v177
	v_med3_f32 v212, v140, s7, v209
	v_med3_f32 v176, v141, s7, v209
	v_cvt_pk_fp8_f32 v212, v212, v176
	v_med3_f32 v176, v142, s7, v209
	v_med3_f32 v177, v143, s7, v209
	v_cvt_pk_fp8_f32 v212, v176, v177 op_sel:[0,0,1]
	v_mfma_f32_16x16x128_f8f6f4 v[176:179], v[0:7], v[72:79], 0
	v_mfma_f32_16x16x128_f8f6f4 v[180:183], v[8:15], v[72:79], 0
	v_med3_f32 v213, v136, s7, v209
	v_med3_f32 v184, v137, s7, v209
	v_cvt_pk_fp8_f32 v213, v213, v184
	v_med3_f32 v184, v138, s7, v209
	v_med3_f32 v185, v139, s7, v209
	v_cvt_pk_fp8_f32 v213, v184, v185 op_sel:[0,0,1]
	v_mfma_f32_16x16x128_f8f6f4 v[184:187], v[16:23], v[72:79], 0
	v_mfma_f32_16x16x128_f8f6f4 v[188:191], v[24:31], v[72:79], 0
	v_lshlrev_b64 v[216:217], 10, v[196:197]
	v_med3_f32 v214, v148, s7, v209
	v_med3_f32 v196, v149, s7, v209
	v_cvt_pk_fp8_f32 v214, v214, v196
	v_lshl_add_u64 v[216:217], v[198:199], 0, v[216:217]
	v_med3_f32 v196, v150, s7, v209
	v_med3_f32 v215, v151, s7, v209
	v_cvt_pk_fp8_f32 v214, v196, v215 op_sel:[0,0,1]
	global_store_dwordx4 v[216:217], v[210:213], off
	v_mfma_f32_16x16x128_f8f6f4 v[160:163], v[32:39], v[80:87], v[160:163]
	v_mfma_f32_16x16x128_f8f6f4 v[164:167], v[40:47], v[80:87], v[164:167]
	v_med3_f32 v215, v144, s7, v209
	v_med3_f32 v196, v145, s7, v209
	v_cvt_pk_fp8_f32 v215, v215, v196
	v_med3_f32 v196, v146, s7, v209
	v_med3_f32 v210, v147, s7, v209
	v_mfma_f32_16x16x128_f8f6f4 v[168:171], v[48:55], v[80:87], v[168:171]
	v_cvt_pk_fp8_f32 v215, v196, v210 op_sel:[0,0,1]
	v_mfma_f32_16x16x128_f8f6f4 v[172:175], v[56:63], v[80:87], v[172:175]
	v_med3_f32 v216, v156, s7, v209
	v_med3_f32 v196, v157, s7, v209
	v_cvt_pk_fp8_f32 v216, v216, v196
	v_med3_f32 v196, v158, s7, v209
	v_med3_f32 v210, v159, s7, v209
	v_mfma_f32_16x16x128_f8f6f4 v[176:179], v[32:39], v[88:95], v[176:179]
	v_cvt_pk_fp8_f32 v216, v196, v210 op_sel:[0,0,1]
	v_mfma_f32_16x16x128_f8f6f4 v[180:183], v[40:47], v[88:95], v[180:183]
	v_med3_f32 v217, v152, s7, v209
	v_med3_f32 v196, v153, s7, v209
	v_cvt_pk_fp8_f32 v217, v217, v196
	v_med3_f32 v196, v154, s7, v209
	v_med3_f32 v210, v155, s7, v209
	v_mfma_f32_16x16x128_f8f6f4 v[184:187], v[48:55], v[88:95], v[184:187]
	v_cvt_pk_fp8_f32 v217, v196, v210 op_sel:[0,0,1]
	v_mfma_f32_16x16x128_f8f6f4 v[188:191], v[56:63], v[88:95], v[188:191]
	v_lshlrev_b64 v[210:211], 10, v[218:219]
	v_lshl_add_u64 v[210:211], v[198:199], 0, v[210:211]
	s_cmp_ge_i32 s19, s25
	global_store_dwordx4 v[210:211], v[214:217], off
	s_cbranch_scc1 .LBB0_774
	s_and_b32 s4, s19, 3
	s_cmp_eq_u32 s4, 0
	s_cbranch_scc1 .LBB0_792
	s_add_i32 s23, s19, s10
	s_cbranch_execz .LBB0_793
	s_branch .LBB0_800
